# P9 ACT stores without the nt hint (acknowledged at L2, so the next unit's first counted waits are not held by store acks); on top of the P9/P10 peeled first K-iteration
# speedup vs baseline: 1.0139x; 1.0063x over previous
.LBB0_1370:
	s_ashr_i32 s37, s36, 31
	s_lshl_b64 s[6:7], s[36:37], 14
	v_lshl_or_b32 v22, s34, 7, v186
	s_add_u32 s6, s10, s6
	s_addc_u32 s7, s11, s7
	v_ashrrev_i32_e32 v23, 31, v22
	s_nop 15
	s_nop 15
	s_mov_b64 s[6:7], 0x2000
	v_lshl_add_u32 v18, v195, 8, v171
	v_or_b32_e32 v24, 16, v18
	v_or_b32_e32 v26, 32, v18
	v_or_b32_e32 v28, 48, v18
	v_ashrrev_i32_e32 v19, 31, v18
	v_ashrrev_i32_e32 v25, 31, v24
	v_ashrrev_i32_e32 v27, 31, v26
	v_ashrrev_i32_e32 v29, 31, v28
	v_lshlrev_b64 v[18:19], 11, v[18:19]
	v_lshlrev_b64 v[24:25], 11, v[24:25]
	v_lshlrev_b64 v[26:27], 11, v[26:27]
	v_lshlrev_b64 v[28:29], 11, v[28:29]
	v_lshl_add_u64 v[18:19], s[14:15], 0, v[18:19]
	v_lshl_add_u64 v[24:25], s[14:15], 0, v[24:25]
	v_lshl_add_u64 v[26:27], s[14:15], 0, v[26:27]
	v_lshl_add_u64 v[28:29], s[14:15], 0, v[28:29]
	v_lshl_add_u64 v[18:19], v[18:19], 0, v[22:23]
	v_lshl_add_u64 v[24:25], v[24:25], 0, v[22:23]
	v_lshl_add_u64 v[26:27], v[26:27], 0, v[22:23]
	v_lshl_add_u64 v[22:23], v[28:29], 0, v[22:23]
	v_mov_b32_e32 v20, v163
	v_mov_b32_e32 v21, v163
	s_mov_b32 s6, 0x40000
	v_mov_b64_e32 v[6:7], v[234:235]
	v_mov_b64_e32 v[8:9], v[236:237]
	v_mov_b64_e32 v[14:15], v[238:239]
	v_mov_b64_e32 v[16:17], v[240:241]
	v_mov_b64_e32 v[10:11], v[242:243]
	v_mov_b64_e32 v[12:13], v[244:245]
	v_mov_b64_e32 v[2:3], v[246:247]
	v_mov_b64_e32 v[4:5], v[248:249]
	v_pk_fma_f32 v[32:33], v[154:155], s[22:23], v[6:7] op_sel_hi:[1,0,1]
	v_pk_fma_f32 v[28:29], v[158:159], s[22:23], v[14:15] op_sel_hi:[1,0,1]
	v_pk_fma_f32 v[154:155], v[156:157], s[22:23], v[8:9] op_sel_hi:[1,0,1]
	v_min_f32_e32 v28, 0x40e00000, v28
	v_min_f32_e32 v29, 0x40e00000, v29
	v_min_f32_e32 v32, 0x40e00000, v32
	v_min_f32_e32 v33, 0x40e00000, v33
	v_pk_mul_f32 v[156:157], v[28:29], s[24:25] op_sel_hi:[1,0]
	v_pk_fma_f32 v[30:31], v[160:161], s[22:23], v[16:17] op_sel_hi:[1,0,1]
	v_pk_mul_f32 v[160:161], v[32:33], s[24:25] op_sel_hi:[1,0]
	v_exp_f32_e32 v156, v156
	v_exp_f32_e32 v157, v157
	v_exp_f32_e32 v160, v160
	v_exp_f32_e32 v161, v161
	v_min_f32_e32 v30, 0x40e00000, v30
	v_min_f32_e32 v31, 0x40e00000, v31
	v_min_f32_e32 v154, 0x40e00000, v154
	v_min_f32_e32 v155, 0x40e00000, v155
	v_pk_mul_f32 v[158:159], v[30:31], s[24:25] op_sel_hi:[1,0]
	v_pk_mul_f32 v[168:169], v[154:155], s[24:25] op_sel_hi:[1,0]
	v_exp_f32_e32 v158, v158
	v_exp_f32_e32 v159, v159
	v_pk_add_f32 v[156:157], v[156:157], 1.0 op_sel_hi:[1,0]
	v_exp_f32_e32 v168, v168
	v_exp_f32_e32 v169, v169
	v_pk_add_f32 v[160:161], v[160:161], 1.0 op_sel_hi:[1,0]
	v_rcp_f32_e32 v156, v156
	v_rcp_f32_e32 v157, v157
	v_rcp_f32_e32 v160, v160
	v_rcp_f32_e32 v161, v161
	v_pk_fma_f32 v[150:151], v[150:151], s[22:23], v[10:11] op_sel_hi:[1,0,1]
	v_pk_fma_f32 v[146:147], v[146:147], s[22:23], v[2:3] op_sel_hi:[1,0,1]
	v_med3_f32 v150, v150, s87, v189
	v_med3_f32 v151, v151, s87, v189
	v_pk_add_f32 v[158:159], v[158:159], 1.0 op_sel_hi:[1,0]
	v_med3_f32 v146, v146, s87, v189
	v_med3_f32 v147, v147, s87, v189
	v_pk_add_f32 v[150:151], v[150:151], 1.0 op_sel_hi:[1,0]
	v_pk_add_f32 v[168:169], v[168:169], 1.0 op_sel_hi:[1,0]
	v_rcp_f32_e32 v158, v158
	v_rcp_f32_e32 v159, v159
	v_pk_mul_f32 v[28:29], v[28:29], v[156:157]
	v_pk_add_f32 v[146:147], v[146:147], 1.0 op_sel_hi:[1,0]
	v_rcp_f32_e32 v168, v168
	v_rcp_f32_e32 v169, v169
	v_pk_mul_f32 v[32:33], v[32:33], v[160:161]
	v_pk_mul_f32 v[28:29], v[150:151], v[28:29]
	v_pk_fma_f32 v[152:153], v[152:153], s[22:23], v[12:13] op_sel_hi:[1,0,1]
	v_pk_mul_f32 v[32:33], v[146:147], v[32:33]
	v_cvt_pk_fp8_f32 v20, v28, v29
	v_pk_fma_f32 v[148:149], v[148:149], s[22:23], v[4:5] op_sel_hi:[1,0,1]
	v_med3_f32 v152, v152, s87, v189
	v_med3_f32 v153, v153, s87, v189
	v_cvt_pk_fp8_f32 v21, v32, v33
	v_med3_f32 v148, v148, s87, v189
	v_med3_f32 v149, v149, s87, v189
	v_pk_add_f32 v[152:153], v[152:153], 1.0 op_sel_hi:[1,0]
	v_pk_mul_f32 v[30:31], v[30:31], v[158:159]
	v_pk_fma_f32 v[142:143], v[142:143], s[22:23], v[14:15] op_sel_hi:[1,0,1]
	v_pk_add_f32 v[148:149], v[148:149], 1.0 op_sel_hi:[1,0]
	v_pk_mul_f32 v[154:155], v[154:155], v[168:169]
	v_pk_mul_f32 v[28:29], v[152:153], v[30:31]
	v_pk_mul_f32 v[30:31], v[148:149], v[154:155]
	v_cvt_pk_fp8_f32 v20, v28, v29 op_sel:[0,0,1]
	v_min_f32_e32 v28, 0x40e00000, v142
	v_min_f32_e32 v29, 0x40e00000, v143
	v_cvt_pk_fp8_f32 v21, v30, v31 op_sel:[0,0,1]
	v_pk_mul_f32 v[30:31], v[28:29], s[24:25] op_sel_hi:[1,0]
	v_pk_fma_f32 v[32:33], v[138:139], s[22:23], v[10:11] op_sel_hi:[1,0,1]
	v_exp_f32_e32 v30, v30
	v_exp_f32_e32 v31, v31
	v_pk_fma_f32 v[138:139], v[144:145], s[22:23], v[16:17] op_sel_hi:[1,0,1]
	v_med3_f32 v32, v32, s87, v189
	v_min_f32_e32 v138, 0x40e00000, v138
	v_pk_add_f32 v[30:31], v[30:31], 1.0 op_sel_hi:[1,0]
	v_min_f32_e32 v139, 0x40e00000, v139
	v_rcp_f32_e32 v30, v30
	v_rcp_f32_e32 v31, v31
	v_pk_mul_f32 v[142:143], v[138:139], s[24:25] op_sel_hi:[1,0]
	v_med3_f32 v33, v33, s87, v189
	v_exp_f32_e32 v142, v142
	v_exp_f32_e32 v143, v143
	v_pk_mul_f32 v[28:29], v[28:29], v[30:31]
	v_pk_add_f32 v[30:31], v[32:33], 1.0 op_sel_hi:[1,0]
	v_pk_fma_f32 v[32:33], v[140:141], s[22:23], v[12:13] op_sel_hi:[1,0,1]
	v_pk_mul_f32 v[30:31], v[30:31], v[28:29]
	v_pk_add_f32 v[28:29], v[142:143], 1.0 op_sel_hi:[1,0]
	v_med3_f32 v32, v32, s87, v189
	v_rcp_f32_e32 v28, v28
	v_rcp_f32_e32 v29, v29
	v_med3_f32 v33, v33, s87, v189
	v_pk_add_f32 v[32:33], v[32:33], 1.0 op_sel_hi:[1,0]
	v_pk_fma_f32 v[136:137], v[136:137], s[22:23], v[8:9] op_sel_hi:[1,0,1]
	v_pk_mul_f32 v[28:29], v[138:139], v[28:29]
	v_min_f32_e32 v136, 0x40e00000, v136
	v_pk_mul_f32 v[32:33], v[32:33], v[28:29]
	v_pk_fma_f32 v[28:29], v[134:135], s[22:23], v[6:7] op_sel_hi:[1,0,1]
	v_min_f32_e32 v137, 0x40e00000, v137
	v_min_f32_e32 v28, 0x40e00000, v28
	v_min_f32_e32 v29, 0x40e00000, v29
	v_pk_mul_f32 v[134:135], v[28:29], s[24:25] op_sel_hi:[1,0]
	v_pk_mul_f32 v[138:139], v[136:137], s[24:25] op_sel_hi:[1,0]
	v_exp_f32_e32 v134, v134
	v_exp_f32_e32 v135, v135
	v_exp_f32_e32 v138, v138
	v_exp_f32_e32 v139, v139
	v_pk_fma_f32 v[130:131], v[130:131], s[22:23], v[2:3] op_sel_hi:[1,0,1]
	v_pk_add_f32 v[134:135], v[134:135], 1.0 op_sel_hi:[1,0]
	v_med3_f32 v130, v130, s87, v189
	v_rcp_f32_e32 v134, v134
	v_rcp_f32_e32 v135, v135
	v_med3_f32 v131, v131, s87, v189
	v_pk_add_f32 v[130:131], v[130:131], 1.0 op_sel_hi:[1,0]
	v_pk_fma_f32 v[132:133], v[132:133], s[22:23], v[4:5] op_sel_hi:[1,0,1]
	v_pk_mul_f32 v[28:29], v[28:29], v[134:135]
	v_med3_f32 v132, v132, s87, v189
	v_pk_mul_f32 v[130:131], v[130:131], v[28:29]
	v_pk_add_f32 v[28:29], v[138:139], 1.0 op_sel_hi:[1,0]
	v_med3_f32 v133, v133, s87, v189
	v_rcp_f32_e32 v28, v28
	v_rcp_f32_e32 v29, v29
	v_pk_fma_f32 v[122:123], v[122:123], s[22:23], v[10:11] op_sel_hi:[1,0,1]
	v_pk_fma_f32 v[118:119], v[118:119], s[22:23], v[6:7] op_sel_hi:[1,0,1]
	v_med3_f32 v122, v122, s87, v189
	v_pk_mul_f32 v[134:135], v[136:137], v[28:29]
	v_mov_b32_e32 v29, v163
	v_cvt_pk_fp8_f32 v29, v130, v131
	v_mov_b32_e32 v28, v163
	v_cvt_pk_fp8_f32 v28, v30, v31
	v_pk_add_f32 v[30:31], v[132:133], 1.0 op_sel_hi:[1,0]
	v_med3_f32 v123, v123, s87, v189
	v_pk_mul_f32 v[30:31], v[30:31], v[134:135]
	v_cvt_pk_fp8_f32 v28, v32, v33 op_sel:[0,0,1]
	v_cvt_pk_fp8_f32 v29, v30, v31 op_sel:[0,0,1]
	v_pk_fma_f32 v[30:31], v[126:127], s[22:23], v[14:15] op_sel_hi:[1,0,1]
	v_pk_fma_f32 v[126:127], v[128:129], s[22:23], v[16:17] op_sel_hi:[1,0,1]
	v_min_f32_e32 v30, 0x40e00000, v30
	v_min_f32_e32 v31, 0x40e00000, v31
	v_pk_mul_f32 v[32:33], v[30:31], s[24:25] op_sel_hi:[1,0]
	v_min_f32_e32 v126, 0x40e00000, v126
	v_exp_f32_e32 v32, v32
	v_exp_f32_e32 v33, v33
	v_min_f32_e32 v127, 0x40e00000, v127
	v_pk_mul_f32 v[128:129], v[126:127], s[24:25] op_sel_hi:[1,0]
	v_min_f32_e32 v118, 0x40e00000, v118
	v_pk_add_f32 v[32:33], v[32:33], 1.0 op_sel_hi:[1,0]
	v_exp_f32_e32 v128, v128
	v_rcp_f32_e32 v32, v32
	v_rcp_f32_e32 v33, v33
	v_exp_f32_e32 v129, v129
	v_min_f32_e32 v119, 0x40e00000, v119
	v_pk_fma_f32 v[120:121], v[120:121], s[22:23], v[8:9] op_sel_hi:[1,0,1]
	v_pk_mul_f32 v[30:31], v[30:31], v[32:33]
	v_pk_add_f32 v[32:33], v[122:123], 1.0 op_sel_hi:[1,0]
	v_pk_fma_f32 v[122:123], v[124:125], s[22:23], v[12:13] op_sel_hi:[1,0,1]
	v_pk_mul_f32 v[30:31], v[32:33], v[30:31]
	v_pk_add_f32 v[32:33], v[128:129], 1.0 op_sel_hi:[1,0]
	v_med3_f32 v122, v122, s87, v189
	v_rcp_f32_e32 v32, v32
	v_rcp_f32_e32 v33, v33
	v_med3_f32 v123, v123, s87, v189
	v_pk_add_f32 v[122:123], v[122:123], 1.0 op_sel_hi:[1,0]
	v_min_f32_e32 v120, 0x40e00000, v120
	v_pk_mul_f32 v[32:33], v[126:127], v[32:33]
	v_min_f32_e32 v121, 0x40e00000, v121
	v_pk_mul_f32 v[32:33], v[122:123], v[32:33]
	v_pk_mul_f32 v[122:123], v[118:119], s[24:25] op_sel_hi:[1,0]
	v_pk_mul_f32 v[124:125], v[120:121], s[24:25] op_sel_hi:[1,0]
	v_exp_f32_e32 v122, v122
	v_exp_f32_e32 v123, v123
	v_exp_f32_e32 v124, v124
	v_exp_f32_e32 v125, v125
	v_pk_fma_f32 v[114:115], v[114:115], s[22:23], v[2:3] op_sel_hi:[1,0,1]
	v_pk_add_f32 v[122:123], v[122:123], 1.0 op_sel_hi:[1,0]
	v_med3_f32 v114, v114, s87, v189
	v_rcp_f32_e32 v122, v122
	v_rcp_f32_e32 v123, v123
	v_med3_f32 v115, v115, s87, v189
	v_pk_add_f32 v[114:115], v[114:115], 1.0 op_sel_hi:[1,0]
	v_pk_fma_f32 v[116:117], v[116:117], s[22:23], v[4:5] op_sel_hi:[1,0,1]
	v_pk_mul_f32 v[118:119], v[118:119], v[122:123]
	v_med3_f32 v116, v116, s87, v189
	v_pk_mul_f32 v[114:115], v[114:115], v[118:119]
	v_pk_add_f32 v[118:119], v[124:125], 1.0 op_sel_hi:[1,0]
	v_med3_f32 v117, v117, s87, v189
	v_rcp_f32_e32 v118, v118
	v_rcp_f32_e32 v119, v119
	v_pk_fma_f32 v[106:107], v[106:107], s[22:23], v[10:11] op_sel_hi:[1,0,1]
	v_pk_fma_f32 v[102:103], v[102:103], s[22:23], v[6:7] op_sel_hi:[1,0,1]
	v_med3_f32 v106, v106, s87, v189
	v_pk_mul_f32 v[118:119], v[120:121], v[118:119]
	v_mov_b32_e32 v121, v163
	v_cvt_pk_fp8_f32 v121, v114, v115
	v_mov_b32_e32 v120, v163
	v_cvt_pk_fp8_f32 v120, v30, v31
	v_pk_add_f32 v[30:31], v[116:117], 1.0 op_sel_hi:[1,0]
	v_med3_f32 v107, v107, s87, v189
	v_pk_mul_f32 v[30:31], v[30:31], v[118:119]
	v_cvt_pk_fp8_f32 v120, v32, v33 op_sel:[0,0,1]
	v_cvt_pk_fp8_f32 v121, v30, v31 op_sel:[0,0,1]
	v_pk_fma_f32 v[30:31], v[110:111], s[22:23], v[14:15] op_sel_hi:[1,0,1]
	v_pk_fma_f32 v[110:111], v[112:113], s[22:23], v[16:17] op_sel_hi:[1,0,1]
	v_min_f32_e32 v30, 0x40e00000, v30
	v_min_f32_e32 v31, 0x40e00000, v31
	v_pk_mul_f32 v[32:33], v[30:31], s[24:25] op_sel_hi:[1,0]
	v_min_f32_e32 v110, 0x40e00000, v110
	v_exp_f32_e32 v32, v32
	v_exp_f32_e32 v33, v33
	v_min_f32_e32 v111, 0x40e00000, v111
	v_pk_mul_f32 v[112:113], v[110:111], s[24:25] op_sel_hi:[1,0]
	v_min_f32_e32 v102, 0x40e00000, v102
	v_pk_add_f32 v[32:33], v[32:33], 1.0 op_sel_hi:[1,0]
	v_exp_f32_e32 v112, v112
	v_rcp_f32_e32 v32, v32
	v_rcp_f32_e32 v33, v33
	v_exp_f32_e32 v113, v113
	v_min_f32_e32 v103, 0x40e00000, v103
	v_pk_fma_f32 v[104:105], v[104:105], s[22:23], v[8:9] op_sel_hi:[1,0,1]
	v_pk_mul_f32 v[30:31], v[30:31], v[32:33]
	v_pk_add_f32 v[32:33], v[106:107], 1.0 op_sel_hi:[1,0]
	v_pk_fma_f32 v[106:107], v[108:109], s[22:23], v[12:13] op_sel_hi:[1,0,1]
	v_pk_mul_f32 v[30:31], v[32:33], v[30:31]
	v_pk_add_f32 v[32:33], v[112:113], 1.0 op_sel_hi:[1,0]
	v_med3_f32 v106, v106, s87, v189
	v_rcp_f32_e32 v32, v32
	v_rcp_f32_e32 v33, v33
	v_med3_f32 v107, v107, s87, v189
	v_pk_add_f32 v[106:107], v[106:107], 1.0 op_sel_hi:[1,0]
	v_min_f32_e32 v104, 0x40e00000, v104
	v_pk_mul_f32 v[32:33], v[110:111], v[32:33]
	v_min_f32_e32 v105, 0x40e00000, v105
	v_pk_mul_f32 v[32:33], v[106:107], v[32:33]
	v_pk_mul_f32 v[106:107], v[102:103], s[24:25] op_sel_hi:[1,0]
	v_pk_mul_f32 v[108:109], v[104:105], s[24:25] op_sel_hi:[1,0]
	v_exp_f32_e32 v106, v106
	v_exp_f32_e32 v107, v107
	v_exp_f32_e32 v108, v108
	v_exp_f32_e32 v109, v109
	v_pk_fma_f32 v[98:99], v[98:99], s[22:23], v[2:3] op_sel_hi:[1,0,1]
	v_pk_add_f32 v[106:107], v[106:107], 1.0 op_sel_hi:[1,0]
	v_med3_f32 v98, v98, s87, v189
	v_rcp_f32_e32 v106, v106
	v_rcp_f32_e32 v107, v107
	v_med3_f32 v99, v99, s87, v189
	v_pk_add_f32 v[98:99], v[98:99], 1.0 op_sel_hi:[1,0]
	v_pk_fma_f32 v[100:101], v[100:101], s[22:23], v[4:5] op_sel_hi:[1,0,1]
	v_pk_mul_f32 v[102:103], v[102:103], v[106:107]
	v_med3_f32 v100, v100, s87, v189
	v_pk_mul_f32 v[98:99], v[98:99], v[102:103]
	v_pk_add_f32 v[102:103], v[108:109], 1.0 op_sel_hi:[1,0]
	v_med3_f32 v101, v101, s87, v189
	v_rcp_f32_e32 v102, v102
	v_rcp_f32_e32 v103, v103
	s_nop 0
	v_pk_mul_f32 v[102:103], v[104:105], v[102:103]
	v_mov_b32_e32 v104, v163
	v_mov_b32_e32 v105, v163
	v_cvt_pk_fp8_f32 v104, v30, v31
	v_cvt_pk_fp8_f32 v105, v98, v99
	v_pk_add_f32 v[30:31], v[100:101], 1.0 op_sel_hi:[1,0]
	v_cvt_pk_fp8_f32 v104, v32, v33 op_sel:[0,0,1]
	v_pk_mul_f32 v[30:31], v[30:31], v[102:103]
	s_nop 0
	v_cvt_pk_fp8_f32 v105, v30, v31 op_sel:[0,0,1]
	global_store_dwordx2 v[18:19], v[20:21], off
	global_store_dwordx2 v[24:25], v[28:29], off
	global_store_dwordx2 v[26:27], v[120:121], off
	global_store_dwordx2 v[22:23], v[104:105], off
	v_pk_fma_f32 v[20:21], v[94:95], s[22:23], v[14:15] op_sel_hi:[1,0,1]
	v_pk_fma_f32 v[26:27], v[96:97], s[22:23], v[16:17] op_sel_hi:[1,0,1]
	v_min_f32_e32 v20, 0x40e00000, v20
	v_min_f32_e32 v21, 0x40e00000, v21
	v_pk_mul_f32 v[22:23], v[20:21], s[24:25] op_sel_hi:[1,0]
	v_min_f32_e32 v26, 0x40e00000, v26
	v_exp_f32_e32 v22, v22
	v_exp_f32_e32 v23, v23
	v_min_f32_e32 v27, 0x40e00000, v27
	v_pk_mul_f32 v[28:29], v[26:27], s[24:25] op_sel_hi:[1,0]
	v_pk_fma_f32 v[24:25], v[90:91], s[22:23], v[10:11] op_sel_hi:[1,0,1]
	v_pk_add_f32 v[22:23], v[22:23], 1.0 op_sel_hi:[1,0]
	v_exp_f32_e32 v28, v28
	v_rcp_f32_e32 v22, v22
	v_rcp_f32_e32 v23, v23
	v_exp_f32_e32 v29, v29
	v_med3_f32 v24, v24, s87, v189
	v_med3_f32 v25, v25, s87, v189
	v_pk_mul_f32 v[20:21], v[20:21], v[22:23]
	v_pk_add_f32 v[22:23], v[24:25], 1.0 op_sel_hi:[1,0]
	v_pk_fma_f32 v[24:25], v[92:93], s[22:23], v[12:13] op_sel_hi:[1,0,1]
	v_pk_mul_f32 v[20:21], v[22:23], v[20:21]
	v_pk_add_f32 v[22:23], v[28:29], 1.0 op_sel_hi:[1,0]
	v_med3_f32 v24, v24, s87, v189
	v_rcp_f32_e32 v22, v22
	v_rcp_f32_e32 v23, v23
	v_med3_f32 v25, v25, s87, v189
	v_pk_add_f32 v[24:25], v[24:25], 1.0 op_sel_hi:[1,0]
	v_pk_fma_f32 v[30:31], v[88:89], s[22:23], v[8:9] op_sel_hi:[1,0,1]
	v_pk_mul_f32 v[22:23], v[26:27], v[22:23]
	v_min_f32_e32 v30, 0x40e00000, v30
	v_pk_mul_f32 v[22:23], v[24:25], v[22:23]
	v_pk_fma_f32 v[24:25], v[86:87], s[22:23], v[6:7] op_sel_hi:[1,0,1]
	v_min_f32_e32 v31, 0x40e00000, v31
	v_min_f32_e32 v24, 0x40e00000, v24
	v_min_f32_e32 v25, 0x40e00000, v25
	v_pk_mul_f32 v[26:27], v[24:25], s[24:25] op_sel_hi:[1,0]
	v_pk_mul_f32 v[32:33], v[30:31], s[24:25] op_sel_hi:[1,0]
	v_exp_f32_e32 v26, v26
	v_exp_f32_e32 v27, v27
	v_exp_f32_e32 v32, v32
	v_exp_f32_e32 v33, v33
	v_pk_fma_f32 v[28:29], v[82:83], s[22:23], v[2:3] op_sel_hi:[1,0,1]
	v_pk_add_f32 v[26:27], v[26:27], 1.0 op_sel_hi:[1,0]
	v_med3_f32 v28, v28, s87, v189
	v_rcp_f32_e32 v26, v26
	v_rcp_f32_e32 v27, v27
	v_med3_f32 v29, v29, s87, v189
	v_pk_mul_f32 v[24:25], v[24:25], v[26:27]
	v_pk_add_f32 v[26:27], v[28:29], 1.0 op_sel_hi:[1,0]
	v_pk_fma_f32 v[28:29], v[84:85], s[22:23], v[4:5] op_sel_hi:[1,0,1]
	v_pk_mul_f32 v[24:25], v[26:27], v[24:25]
	v_pk_add_f32 v[26:27], v[32:33], 1.0 op_sel_hi:[1,0]
	v_med3_f32 v28, v28, s87, v189
	v_rcp_f32_e32 v26, v26
	v_rcp_f32_e32 v27, v27
	v_med3_f32 v29, v29, s87, v189
	v_pk_mul_f32 v[26:27], v[30:31], v[26:27]
	v_mov_b32_e32 v30, v163
	v_mov_b32_e32 v31, v163
	v_cvt_pk_fp8_f32 v30, v20, v21
	v_cvt_pk_fp8_f32 v31, v24, v25
	v_pk_add_f32 v[20:21], v[28:29], 1.0 op_sel_hi:[1,0]
	v_pk_fma_f32 v[24:25], v[74:75], s[22:23], v[10:11] op_sel_hi:[1,0,1]
	v_pk_mul_f32 v[20:21], v[20:21], v[26:27]
	v_cvt_pk_fp8_f32 v30, v22, v23 op_sel:[0,0,1]
	v_cvt_pk_fp8_f32 v31, v20, v21 op_sel:[0,0,1]
	v_add_co_u32_e32 v20, vcc, s6, v18
	v_pk_fma_f32 v[26:27], v[80:81], s[22:23], v[16:17] op_sel_hi:[1,0,1]
	s_nop 0
	v_addc_co_u32_e32 v21, vcc, 0, v19, vcc
	global_store_dwordx2 v[20:21], v[30:31], off
	v_pk_fma_f32 v[20:21], v[78:79], s[22:23], v[14:15] op_sel_hi:[1,0,1]
	v_min_f32_e32 v26, 0x40e00000, v26
	v_min_f32_e32 v20, 0x40e00000, v20
	v_min_f32_e32 v21, 0x40e00000, v21
	v_pk_mul_f32 v[22:23], v[20:21], s[24:25] op_sel_hi:[1,0]
	v_min_f32_e32 v27, 0x40e00000, v27
	v_exp_f32_e32 v22, v22
	v_exp_f32_e32 v23, v23
	v_pk_mul_f32 v[28:29], v[26:27], s[24:25] op_sel_hi:[1,0]
	v_med3_f32 v24, v24, s87, v189
	v_exp_f32_e32 v28, v28
	v_pk_add_f32 v[22:23], v[22:23], 1.0 op_sel_hi:[1,0]
	v_exp_f32_e32 v29, v29
	v_rcp_f32_e32 v22, v22
	v_rcp_f32_e32 v23, v23
	v_med3_f32 v25, v25, s87, v189
	v_pk_fma_f32 v[30:31], v[72:73], s[22:23], v[8:9] op_sel_hi:[1,0,1]
	s_mov_b32 s6, 0x48000
	v_pk_mul_f32 v[20:21], v[20:21], v[22:23]
	v_pk_add_f32 v[22:23], v[24:25], 1.0 op_sel_hi:[1,0]
	v_pk_fma_f32 v[24:25], v[76:77], s[22:23], v[12:13] op_sel_hi:[1,0,1]
	v_pk_mul_f32 v[20:21], v[22:23], v[20:21]
	v_pk_add_f32 v[22:23], v[28:29], 1.0 op_sel_hi:[1,0]
	v_med3_f32 v24, v24, s87, v189
	v_rcp_f32_e32 v22, v22
	v_rcp_f32_e32 v23, v23
	v_med3_f32 v25, v25, s87, v189
	v_pk_add_f32 v[24:25], v[24:25], 1.0 op_sel_hi:[1,0]
	v_min_f32_e32 v30, 0x40e00000, v30
	v_pk_mul_f32 v[22:23], v[26:27], v[22:23]
	v_min_f32_e32 v31, 0x40e00000, v31
	v_pk_mul_f32 v[22:23], v[24:25], v[22:23]
	v_pk_fma_f32 v[24:25], v[70:71], s[22:23], v[6:7] op_sel_hi:[1,0,1]
	v_pk_mul_f32 v[32:33], v[30:31], s[24:25] op_sel_hi:[1,0]
	v_min_f32_e32 v24, 0x40e00000, v24
	v_min_f32_e32 v25, 0x40e00000, v25
	v_pk_mul_f32 v[26:27], v[24:25], s[24:25] op_sel_hi:[1,0]
	v_exp_f32_e32 v32, v32
	v_exp_f32_e32 v26, v26
	v_exp_f32_e32 v27, v27
	v_exp_f32_e32 v33, v33
	v_pk_fma_f32 v[28:29], v[66:67], s[22:23], v[2:3] op_sel_hi:[1,0,1]
	v_pk_add_f32 v[26:27], v[26:27], 1.0 op_sel_hi:[1,0]
	s_nop 0
	v_rcp_f32_e32 v26, v26
	v_rcp_f32_e32 v27, v27
	v_med3_f32 v28, v28, s87, v189
	v_med3_f32 v29, v29, s87, v189
	v_pk_mul_f32 v[24:25], v[24:25], v[26:27]
	v_pk_add_f32 v[26:27], v[28:29], 1.0 op_sel_hi:[1,0]
	v_pk_fma_f32 v[28:29], v[68:69], s[22:23], v[4:5] op_sel_hi:[1,0,1]
	v_pk_mul_f32 v[24:25], v[26:27], v[24:25]
	v_pk_add_f32 v[26:27], v[32:33], 1.0 op_sel_hi:[1,0]
	v_med3_f32 v28, v28, s87, v189
	v_rcp_f32_e32 v26, v26
	v_rcp_f32_e32 v27, v27
	v_med3_f32 v29, v29, s87, v189
	v_pk_mul_f32 v[26:27], v[30:31], v[26:27]
	v_mov_b32_e32 v30, v163
	v_mov_b32_e32 v31, v163
	v_cvt_pk_fp8_f32 v30, v20, v21
	v_cvt_pk_fp8_f32 v31, v24, v25
	v_pk_add_f32 v[20:21], v[28:29], 1.0 op_sel_hi:[1,0]
	v_pk_fma_f32 v[24:25], v[58:59], s[22:23], v[10:11] op_sel_hi:[1,0,1]
	v_pk_mul_f32 v[20:21], v[20:21], v[26:27]
	v_cvt_pk_fp8_f32 v30, v22, v23 op_sel:[0,0,1]
	v_cvt_pk_fp8_f32 v31, v20, v21 op_sel:[0,0,1]
	v_add_co_u32_e32 v20, vcc, s6, v18
	v_pk_fma_f32 v[26:27], v[64:65], s[22:23], v[16:17] op_sel_hi:[1,0,1]
	s_nop 0
	v_addc_co_u32_e32 v21, vcc, 0, v19, vcc
	global_store_dwordx2 v[20:21], v[30:31], off
	v_pk_fma_f32 v[20:21], v[62:63], s[22:23], v[14:15] op_sel_hi:[1,0,1]
	v_min_f32_e32 v26, 0x40e00000, v26
	v_min_f32_e32 v20, 0x40e00000, v20
	v_min_f32_e32 v21, 0x40e00000, v21
	v_pk_mul_f32 v[22:23], v[20:21], s[24:25] op_sel_hi:[1,0]
	v_min_f32_e32 v27, 0x40e00000, v27
	v_exp_f32_e32 v22, v22
	v_exp_f32_e32 v23, v23
	v_pk_mul_f32 v[28:29], v[26:27], s[24:25] op_sel_hi:[1,0]
	v_med3_f32 v24, v24, s87, v189
	v_exp_f32_e32 v28, v28
	v_pk_add_f32 v[22:23], v[22:23], 1.0 op_sel_hi:[1,0]
	v_exp_f32_e32 v29, v29
	v_rcp_f32_e32 v22, v22
	v_rcp_f32_e32 v23, v23
	v_med3_f32 v25, v25, s87, v189
	v_pk_fma_f32 v[30:31], v[56:57], s[22:23], v[8:9] op_sel_hi:[1,0,1]
	s_mov_b32 s6, 0x50000
	v_pk_mul_f32 v[20:21], v[20:21], v[22:23]
	v_pk_add_f32 v[22:23], v[24:25], 1.0 op_sel_hi:[1,0]
	v_pk_fma_f32 v[24:25], v[60:61], s[22:23], v[12:13] op_sel_hi:[1,0,1]
	v_pk_mul_f32 v[20:21], v[22:23], v[20:21]
	v_pk_add_f32 v[22:23], v[28:29], 1.0 op_sel_hi:[1,0]
	v_med3_f32 v24, v24, s87, v189
	v_rcp_f32_e32 v22, v22
	v_rcp_f32_e32 v23, v23
	v_med3_f32 v25, v25, s87, v189
	v_pk_add_f32 v[24:25], v[24:25], 1.0 op_sel_hi:[1,0]
	v_min_f32_e32 v30, 0x40e00000, v30
	v_pk_mul_f32 v[22:23], v[26:27], v[22:23]
	v_min_f32_e32 v31, 0x40e00000, v31
	v_pk_mul_f32 v[22:23], v[24:25], v[22:23]
	v_pk_fma_f32 v[24:25], v[54:55], s[22:23], v[6:7] op_sel_hi:[1,0,1]
	v_pk_mul_f32 v[32:33], v[30:31], s[24:25] op_sel_hi:[1,0]
	v_min_f32_e32 v24, 0x40e00000, v24
	v_min_f32_e32 v25, 0x40e00000, v25
	v_pk_mul_f32 v[26:27], v[24:25], s[24:25] op_sel_hi:[1,0]
	v_exp_f32_e32 v32, v32
	v_exp_f32_e32 v26, v26
	v_exp_f32_e32 v27, v27
	v_exp_f32_e32 v33, v33
	v_pk_fma_f32 v[28:29], v[50:51], s[22:23], v[2:3] op_sel_hi:[1,0,1]
	v_pk_fma_f32 v[14:15], v[46:47], s[22:23], v[14:15] op_sel_hi:[1,0,1]
	v_pk_add_f32 v[26:27], v[26:27], 1.0 op_sel_hi:[1,0]
	v_med3_f32 v28, v28, s87, v189
	v_rcp_f32_e32 v26, v26
	v_rcp_f32_e32 v27, v27
	v_med3_f32 v29, v29, s87, v189
	v_min_f32_e32 v14, 0x40e00000, v14
	v_min_f32_e32 v15, 0x40e00000, v15
	v_pk_mul_f32 v[24:25], v[24:25], v[26:27]
	v_pk_add_f32 v[26:27], v[28:29], 1.0 op_sel_hi:[1,0]
	v_pk_fma_f32 v[28:29], v[52:53], s[22:23], v[4:5] op_sel_hi:[1,0,1]
	v_pk_mul_f32 v[24:25], v[26:27], v[24:25]
	v_pk_add_f32 v[26:27], v[32:33], 1.0 op_sel_hi:[1,0]
	v_med3_f32 v28, v28, s87, v189
	v_rcp_f32_e32 v26, v26
	v_rcp_f32_e32 v27, v27
	v_med3_f32 v29, v29, s87, v189
	v_pk_fma_f32 v[16:17], v[48:49], s[22:23], v[16:17] op_sel_hi:[1,0,1]
	v_pk_fma_f32 v[10:11], v[42:43], s[22:23], v[10:11] op_sel_hi:[1,0,1]
	v_pk_mul_f32 v[26:27], v[30:31], v[26:27]
	v_mov_b32_e32 v30, v163
	v_mov_b32_e32 v31, v163
	v_cvt_pk_fp8_f32 v30, v20, v21
	v_cvt_pk_fp8_f32 v31, v24, v25
	v_pk_add_f32 v[20:21], v[28:29], 1.0 op_sel_hi:[1,0]
	v_min_f32_e32 v16, 0x40e00000, v16
	v_pk_mul_f32 v[20:21], v[20:21], v[26:27]
	v_cvt_pk_fp8_f32 v30, v22, v23 op_sel:[0,0,1]
	v_cvt_pk_fp8_f32 v31, v20, v21 op_sel:[0,0,1]
	v_add_co_u32_e32 v20, vcc, s6, v18
	v_min_f32_e32 v17, 0x40e00000, v17
	s_nop 0
	v_addc_co_u32_e32 v21, vcc, 0, v19, vcc
	global_store_dwordx2 v[20:21], v[30:31], off
	v_pk_mul_f32 v[20:21], v[14:15], s[24:25] op_sel_hi:[1,0]
	v_pk_mul_f32 v[22:23], v[16:17], s[24:25] op_sel_hi:[1,0]
	v_exp_f32_e32 v20, v20
	v_exp_f32_e32 v21, v21
	v_exp_f32_e32 v22, v22
	v_exp_f32_e32 v23, v23
	v_med3_f32 v10, v10, s87, v189
	v_pk_add_f32 v[20:21], v[20:21], 1.0 op_sel_hi:[1,0]
	v_med3_f32 v11, v11, s87, v189
	v_rcp_f32_e32 v20, v20
	v_rcp_f32_e32 v21, v21
	v_pk_add_f32 v[10:11], v[10:11], 1.0 op_sel_hi:[1,0]
	v_pk_fma_f32 v[12:13], v[44:45], s[22:23], v[12:13] op_sel_hi:[1,0,1]
	v_pk_fma_f32 v[6:7], v[38:39], s[22:23], v[6:7] op_sel_hi:[1,0,1]
	v_pk_mul_f32 v[14:15], v[14:15], v[20:21]
	v_med3_f32 v12, v12, s87, v189
	v_pk_mul_f32 v[10:11], v[10:11], v[14:15]
	v_pk_add_f32 v[14:15], v[22:23], 1.0 op_sel_hi:[1,0]
	v_med3_f32 v13, v13, s87, v189
	v_rcp_f32_e32 v14, v14
	v_rcp_f32_e32 v15, v15
	v_pk_add_f32 v[12:13], v[12:13], 1.0 op_sel_hi:[1,0]
	v_min_f32_e32 v6, 0x40e00000, v6
	v_min_f32_e32 v7, 0x40e00000, v7
	v_pk_mul_f32 v[14:15], v[16:17], v[14:15]
	v_pk_fma_f32 v[8:9], v[40:41], s[22:23], v[8:9] op_sel_hi:[1,0,1]
	v_pk_mul_f32 v[12:13], v[12:13], v[14:15]
	v_pk_mul_f32 v[14:15], v[6:7], s[24:25] op_sel_hi:[1,0]
	v_min_f32_e32 v8, 0x40e00000, v8
	v_exp_f32_e32 v14, v14
	v_exp_f32_e32 v15, v15
	v_min_f32_e32 v9, 0x40e00000, v9
	v_pk_mul_f32 v[16:17], v[8:9], s[24:25] op_sel_hi:[1,0]
	v_pk_fma_f32 v[2:3], v[34:35], s[22:23], v[2:3] op_sel_hi:[1,0,1]
	v_pk_add_f32 v[14:15], v[14:15], 1.0 op_sel_hi:[1,0]
	v_exp_f32_e32 v16, v16
	v_rcp_f32_e32 v14, v14
	v_rcp_f32_e32 v15, v15
	v_exp_f32_e32 v17, v17
	v_med3_f32 v2, v2, s87, v189
	v_med3_f32 v3, v3, s87, v189
	v_pk_mul_f32 v[6:7], v[6:7], v[14:15]
	v_pk_add_f32 v[2:3], v[2:3], 1.0 op_sel_hi:[1,0]
	v_pk_fma_f32 v[4:5], v[36:37], s[22:23], v[4:5] op_sel_hi:[1,0,1]
	v_pk_mul_f32 v[2:3], v[2:3], v[6:7]
	v_pk_add_f32 v[6:7], v[16:17], 1.0 op_sel_hi:[1,0]
	v_med3_f32 v4, v4, s87, v189
	v_rcp_f32_e32 v6, v6
	v_rcp_f32_e32 v7, v7
	v_med3_f32 v5, v5, s87, v189
	v_pk_mul_f32 v[6:7], v[8:9], v[6:7]
	v_mov_b32_e32 v8, v163
	v_mov_b32_e32 v9, v163
	v_cvt_pk_fp8_f32 v8, v10, v11
	v_cvt_pk_fp8_f32 v9, v2, v3
	v_pk_add_f32 v[2:3], v[4:5], 1.0 op_sel_hi:[1,0]
	v_cvt_pk_fp8_f32 v8, v12, v13 op_sel:[0,0,1]
	v_pk_mul_f32 v[2:3], v[2:3], v[6:7]
	s_nop 0
	v_cvt_pk_fp8_f32 v9, v2, v3 op_sel:[0,0,1]
	v_add_co_u32_e32 v2, vcc, 0x58000, v18
	s_nop 1
	v_addc_co_u32_e32 v3, vcc, 0, v19, vcc
	s_andn2_b64 vcc, exec, s[4:5]
	s_mov_b64 s[4:5], -1
	global_store_dwordx2 v[2:3], v[8:9], off
	s_cbranch_vccnz .LBB0_1348
	s_andn2_b64 vcc, exec, s[12:13]
	s_cbranch_vccnz .LBB0_1347
	s_barrier
	s_branch .LBB0_1347
